# static s_setprio 1 for waves 4-7 also in the attention phase's conv rows and in the convert_in_tail loops (on top of PEER and LN)
# baseline (speedup 1.0000x reference)
.LBB0_360:
	v_readlane_b32 s4, v254, 46
	s_sub_i32 s6, s37, s4
	s_cmp_gt_i32 s6, 0
	s_cselect_b64 s[4:5], -1, 0
	s_cmp_lt_i32 s6, s33
	s_cselect_b64 s[8:9], -1, 0
	s_and_b64 s[4:5], s[4:5], s[8:9]
	s_and_b64 s[4:5], s[4:5], exec
	s_cselect_b32 s5, s6, 0
	s_sub_i32 s4, s76, s5
	s_cmp_lt_i32 s4, 0
	s_cbranch_scc1 .LBB0_369
	s_sub_i32 s5, s33, s5
	s_lshl_b32 s5, s5, 3
	s_abs_i32 s6, s5
	v_cvt_f32_u32_e32 v2, s6
	s_ashr_i32 s8, s27, 6
	s_sub_i32 s27, 0, s6
	s_add_i32 s9, s26, s5
	v_rcp_iflag_f32_e32 v2, v2
	s_add_i32 s9, s9, -1
	s_xor_b32 s5, s9, s5
	s_abs_i32 s9, s9
	v_mul_f32_e32 v2, 0x4f7ffffe, v2
	v_cvt_u32_f32_e32 v2, v2
	s_ashr_i32 s5, s5, 31
	v_readfirstlane_b32 s37, v2
	s_mul_i32 s27, s27, s37
	s_mul_hi_u32 s27, s37, s27
	s_add_i32 s37, s37, s27
	s_mul_hi_u32 s27, s9, s37
	s_mul_i32 s37, s27, s6
	s_sub_i32 s9, s9, s37
	s_add_i32 s40, s27, 1
	s_sub_i32 s37, s9, s6
	s_cmp_ge_u32 s9, s6
	s_cselect_b32 s27, s40, s27
	s_cselect_b32 s9, s37, s9
	s_add_i32 s37, s27, 1
	s_cmp_ge_u32 s9, s6
	s_cselect_b32 s6, s37, s27
	s_xor_b32 s6, s6, s5
	s_lshl_b32 s4, s4, 3
	s_sub_i32 s5, s6, s5
	s_add_i32 s4, s4, s8
	s_mul_i32 s4, s5, s4
	s_add_i32 s5, s4, s5
	s_min_i32 s6, s5, s26
	s_cmp_ge_i32 s4, s6
	s_cbranch_scc1 .LBB0_369
	s_cmp_gt_u32 s8, 3
	s_cbranch_scc0 .Lcv_lowprio
	s_setprio 1
.Lcv_lowprio:
	s_nop 0
	s_cmpk_lt_i32 s4, 0x4000
	s_movk_i32 s5, 0x1fff
	s_cselect_b32 s5, s5, 0xff
	s_and_b32 s5, s5, s4
	s_cmp_lg_u32 s5, 0
	v_lshlrev_b32_e32 v2, 3, v185
	s_cbranch_scc0 .LBB0_381
	s_load_dwordx2 s[8:9], s[0:1], 0xa8
	s_add_i32 s5, s4, -1
	s_mul_hi_i32 s27, s5, 0x2400
	s_mulk_i32 s5, 0x2400
	v_lshlrev_b32_e32 v4, 4, v185
	s_waitcnt lgkmcnt(0)
	s_add_u32 s8, s8, s5
	s_addc_u32 s9, s9, s27
	v_mov_b32_e32 v5, v3
	v_lshl_add_u64 v[8:9], s[8:9], 0, v[4:5]
	s_mov_b64 s[8:9], 0x17600000
	v_lshl_add_u64 v[12:13], v[8:9], 0, s[8:9]
	s_mov_b32 s5, 0x17601000
	global_load_dwordx4 v[4:7], v[12:13], off offset:2048
	v_add_co_u32_e32 v16, vcc, s5, v8
	s_nop 1
	v_addc_co_u32_e32 v17, vcc, 0, v9, vcc
	global_load_dwordx4 v[8:11], v[16:17], off
	s_nop 0
	global_load_dwordx4 v[12:15], v[12:13], off offset:3072
	s_nop 0
	global_load_dwordx4 v[16:19], v[16:17], off offset:1024
	s_waitcnt vmcnt(3)
	v_lshlrev_b32_e32 v20, 16, v4
	v_and_b32_e32 v21, 0xffff0000, v4
	v_lshlrev_b32_e32 v4, 16, v5
	v_and_b32_e32 v5, 0xffff0000, v5
	s_waitcnt vmcnt(2)
	v_lshlrev_b32_e32 v22, 16, v8
	v_and_b32_e32 v23, 0xffff0000, v8
	v_lshlrev_b32_e32 v8, 16, v9
	v_and_b32_e32 v9, 0xffff0000, v9
	v_pk_mul_f32 v[112:113], v[4:5], v[8:9]
	v_lshlrev_b32_e32 v4, 16, v6
	v_and_b32_e32 v5, 0xffff0000, v6
	v_lshlrev_b32_e32 v8, 16, v10
	v_and_b32_e32 v9, 0xffff0000, v10
	v_pk_mul_f32 v[110:111], v[4:5], v[8:9]
	v_lshlrev_b32_e32 v4, 16, v7
	v_and_b32_e32 v5, 0xffff0000, v7
	v_lshlrev_b32_e32 v6, 16, v11
	v_and_b32_e32 v7, 0xffff0000, v11
	v_pk_mul_f32 v[108:109], v[4:5], v[6:7]
	s_waitcnt vmcnt(1)
	v_lshlrev_b32_e32 v4, 16, v12
	v_and_b32_e32 v5, 0xffff0000, v12
	s_waitcnt vmcnt(0)
	v_lshlrev_b32_e32 v6, 16, v16
	v_and_b32_e32 v7, 0xffff0000, v16
	v_pk_mul_f32 v[106:107], v[4:5], v[6:7]
	v_lshlrev_b32_e32 v4, 16, v13
	v_and_b32_e32 v5, 0xffff0000, v13
	v_lshlrev_b32_e32 v6, 16, v17
	v_and_b32_e32 v7, 0xffff0000, v17
	v_pk_mul_f32 v[104:105], v[4:5], v[6:7]
	v_lshlrev_b32_e32 v4, 16, v14
	v_and_b32_e32 v5, 0xffff0000, v14
	v_lshlrev_b32_e32 v6, 16, v18
	v_and_b32_e32 v7, 0xffff0000, v18
	v_pk_mul_f32 v[102:103], v[4:5], v[6:7]
	v_lshlrev_b32_e32 v4, 16, v15
	v_and_b32_e32 v5, 0xffff0000, v15
	v_lshlrev_b32_e32 v6, 16, v19
	v_and_b32_e32 v7, 0xffff0000, v19
	v_pk_mul_f32 v[114:115], v[20:21], v[22:23]
	v_pk_mul_f32 v[100:101], v[4:5], v[6:7]
	v_mov_b32_e32 v118, v103
	v_mov_b32_e32 v116, v101
	v_mov_b32_e32 v120, v105
	v_mov_b32_e32 v122, v107
	v_mov_b32_e32 v124, v109
	v_mov_b32_e32 v128, v111
	v_mov_b32_e32 v132, v113
	v_mov_b32_e32 v144, v115
	s_cbranch_execnz .LBB0_365

.LBB0_420:
	s_setprio 0
	s_nop 0
	s_cmp_le_i32 s68, s6
	s_cselect_b64 s[0:1], -1, 0
	s_cmp_lt_i32 s6, s69
	s_cselect_b64 s[4:5], -1, 0
	s_and_b64 s[4:5], s[0:1], s[4:5]
	s_mov_b64 s[0:1], -1
	s_and_b64 vcc, exec, s[4:5]
	s_cbranch_vccnz .LBB0_422
	s_mul_i32 s0, s36, 6
	s_add_i32 s6, s0, 5
	s_mov_b64 s[0:1], 0

.LBB0_439:
	s_and_b64 vcc, exec, s[4:5]
	s_cbranch_vccz .LBB0_450
	s_ashr_i32 s37, s1, 6
	s_cmp_gt_u32 s37, 3
	s_cbranch_scc0 .Lct1_lowprio
	s_setprio 1
.Lct1_lowprio:
	s_nop 0
	s_lshr_b32 s4, s0, 3
	s_mul_i32 s4, s4, s37
	s_lshr_b32 s27, s27, 3
	s_add_i32 s27, s27, s4
	s_mov_b32 s1, s27
	s_mov_b32 s37, 0
	s_nop 0
	s_cmpk_gt_i32 s1, 0x1fff
	s_cbranch_scc1 .LBB0_450
	s_lshl_b32 s4, s36, 14
	s_load_dwordx4 s[44:47], s[8:9], 0x80
	s_load_dwordx2 s[50:51], s[8:9], 0xa8
	s_add_i32 s6, s4, 0x6000
	s_add_i32 s4, s4, s1
	s_addk_i32 s4, 0x4000
	s_ashr_i32 s5, s4, 31
	s_lshl_b64 s[8:9], s[4:5], 13
	s_waitcnt vmcnt(0)
	v_and_b32_e32 v18, 63, v2
	s_waitcnt lgkmcnt(0)
	s_add_u32 s40, s44, s8
	s_addc_u32 s41, s45, s9
	v_lshlrev_b32_e32 v2, 5, v18
	v_lshl_add_u64 v[4:5], s[40:41], 0, v[2:3]
	v_add_co_u32_e32 v8, vcc, s77, v4
	s_add_u32 s8, s46, s8
	global_load_dwordx4 v[124:127], v2, s[40:41] offset:16 nt
	global_load_dwordx4 v[128:131], v2, s[40:41] nt
	global_load_dwordx4 v[116:119], v2, s[40:41] offset:2064 nt
	global_load_dwordx4 v[120:123], v2, s[40:41] offset:2048 nt
	s_mov_b64 s[40:41], 0x1000
	v_addc_co_u32_e32 v9, vcc, 0, v5, vcc
	s_mov_b64 s[42:43], 0x1800
	s_addc_u32 s9, s47, s9
	v_lshl_add_u64 v[6:7], v[4:5], 0, s[40:41]
	global_load_dwordx4 v[112:115], v[8:9], off nt
	global_load_dwordx4 v[108:111], v[6:7], off offset:16 nt
	v_lshl_add_u64 v[4:5], v[4:5], 0, s[42:43]
	global_load_dwordx4 v[104:107], v[8:9], off offset:2048 nt
	global_load_dwordx4 v[100:103], v[4:5], off offset:16 nt
	v_lshl_add_u64 v[8:9], s[8:9], 0, v[2:3]
	global_load_dwordx4 v[24:27], v2, s[8:9] offset:16 nt
	global_load_dwordx4 v[40:43], v2, s[8:9] nt
	global_load_dwordx4 v[4:7], v2, s[8:9] offset:2064 nt
	global_load_dwordx4 v[28:31], v2, s[8:9] offset:2048 nt
	v_add_co_u32_e32 v16, vcc, s77, v8
	v_lshl_add_u64 v[10:11], v[8:9], 0, s[40:41]
	s_nop 0
	v_addc_co_u32_e32 v17, vcc, 0, v9, vcc
	v_lshl_add_u64 v[8:9], v[8:9], 0, s[42:43]
	global_load_dwordx4 v[36:39], v[16:17], off nt
	global_load_dwordx4 v[12:15], v[10:11], off offset:16 nt
	global_load_dwordx4 v[32:35], v[16:17], off offset:2048 nt
	s_nop 0
	global_load_dwordx4 v[8:11], v[8:9], off offset:16 nt
	s_add_i32 s8, s1, s85
	s_ashr_i32 s9, s8, 31
	s_add_i32 s5, s27, s0
	s_lshl_b64 s[52:53], s[8:9], 3
	s_lshl_b64 s[8:9], s[8:9], 10
	s_add_i32 s5, s5, s37
	v_lshl_or_b32 v132, v18, 2, s8
	s_add_i32 s8, s5, s85
	s_ashr_i32 s1, s0, 31
	v_mov_b32_e32 v133, s9
	s_ashr_i32 s9, s8, 31
	s_lshl_b64 s[54:55], s[0:1], 3
	s_lshl_b64 s[56:57], s[0:1], 10
	s_lshl_b64 s[8:9], s[8:9], 13
	s_add_u32 s46, s46, s8
	s_addc_u32 s47, s47, s9
	s_lshl_b64 s[58:59], s[0:1], 13
	s_add_u32 s44, s44, s8
	v_cmp_eq_u32_e64 s[40:41], 0, v18
	s_addc_u32 s45, s45, s9
	s_branch .LBB0_443

.LBB0_450:
	s_setprio 0
	s_nop 0
	s_mul_i32 s0, s36, 6
	s_add_i32 s6, s0, 5
	s_cmp_ge_i32 s6, s69
	s_cbranch_scc1 .LBB0_500
	s_waitcnt vmcnt(0)
	s_waitcnt vmcnt(0)
	s_barrier
	s_mov_b64 s[0:1], exec
	v_readlane_b32 s4, v253, 16
	v_readlane_b32 s5, v253, 17
	s_and_b64 s[4:5], s[0:1], s[4:5]
	s_mov_b64 exec, s[4:5]
	s_cbranch_execz .LBB0_499
	v_readlane_b32 s4, v254, 2
	s_waitcnt vmcnt(0) expcnt(0) lgkmcnt(0)
	s_nop 0
	v_mov_b32_e32 v2, s4
	ds_read_b32 v5, v2
	ds_read_b32 v4, v2 offset:4
	s_waitcnt lgkmcnt(1)
	v_cmp_ne_u32_e32 vcc, 0, v5
	s_cbranch_vccnz .LBB0_467
	v_readlane_b32 s8, v254, 0
	v_readlane_b32 s9, v254, 1
	s_load_dwordx2 s[4:5], s[8:9], 0x4
	s_mov_b32 s37, 1
	s_waitcnt lgkmcnt(0)
	s_mul_i32 s27, s4, s33
	s_mul_i32 s27, s27, s5
	s_branch .LBB0_455

.Lct0_lowprio:
	s_nop 0
	s_lshr_b32 s4, s0, 3
	s_mul_i32 s4, s4, s37
	s_lshr_b32 s27, s27, 3
	s_add_i32 s27, s27, s4
	s_mov_b32 s1, s27
	s_mov_b32 s37, 0
	s_nop 0
	s_cmpk_gt_i32 s1, 0x1fff
	s_cbranch_scc1 .LBB0_625
	s_lshl_b32 s4, s36, 14
	s_load_dwordx4 s[44:47], s[8:9], 0x80
	s_load_dwordx2 s[48:49], s[8:9], 0xa8
	s_add_i32 s6, s4, 0x8000
	s_add_i32 s4, s4, s1
	s_addk_i32 s4, 0x6000
	s_ashr_i32 s5, s4, 31
	s_lshl_b64 s[8:9], s[4:5], 13
	s_waitcnt vmcnt(0)
	v_and_b32_e32 v18, 63, v2
	s_waitcnt lgkmcnt(0)
	s_add_u32 s40, s44, s8
	s_addc_u32 s41, s45, s9
	v_lshlrev_b32_e32 v2, 5, v18
	v_lshl_add_u64 v[4:5], s[40:41], 0, v[2:3]
	v_add_co_u32_e32 v8, vcc, s77, v4
	s_add_u32 s8, s46, s8
	global_load_dwordx4 v[124:127], v2, s[40:41] offset:16 nt
	global_load_dwordx4 v[128:131], v2, s[40:41] nt
	global_load_dwordx4 v[116:119], v2, s[40:41] offset:2064 nt
	global_load_dwordx4 v[120:123], v2, s[40:41] offset:2048 nt
	s_mov_b64 s[40:41], 0x1000
	v_addc_co_u32_e32 v9, vcc, 0, v5, vcc
	s_mov_b64 s[42:43], 0x1800
	s_addc_u32 s9, s47, s9
	v_lshl_add_u64 v[6:7], v[4:5], 0, s[40:41]
	global_load_dwordx4 v[112:115], v[8:9], off nt
	global_load_dwordx4 v[108:111], v[6:7], off offset:16 nt
	v_lshl_add_u64 v[4:5], v[4:5], 0, s[42:43]
	global_load_dwordx4 v[104:107], v[8:9], off offset:2048 nt
	global_load_dwordx4 v[100:103], v[4:5], off offset:16 nt
	v_lshl_add_u64 v[8:9], s[8:9], 0, v[2:3]
	global_load_dwordx4 v[24:27], v2, s[8:9] offset:16 nt
	global_load_dwordx4 v[40:43], v2, s[8:9] nt
	global_load_dwordx4 v[4:7], v2, s[8:9] offset:2064 nt
	global_load_dwordx4 v[28:31], v2, s[8:9] offset:2048 nt
	v_add_co_u32_e32 v16, vcc, s77, v8
	v_lshl_add_u64 v[10:11], v[8:9], 0, s[40:41]
	s_nop 0
	v_addc_co_u32_e32 v17, vcc, 0, v9, vcc
	v_lshl_add_u64 v[8:9], v[8:9], 0, s[42:43]
	global_load_dwordx4 v[36:39], v[16:17], off nt
	global_load_dwordx4 v[12:15], v[10:11], off offset:16 nt
	global_load_dwordx4 v[32:35], v[16:17], off offset:2048 nt
	s_nop 0
	global_load_dwordx4 v[8:11], v[8:9], off offset:16 nt
	v_readlane_b32 s42, v253, 12
	s_add_i32 s8, s1, s42
	s_ashr_i32 s9, s8, 31
	s_add_i32 s5, s27, s0
	s_lshl_b64 s[50:51], s[8:9], 3
	s_lshl_b64 s[8:9], s[8:9], 10
	s_add_i32 s5, s5, s37
	v_lshl_or_b32 v132, v18, 2, s8
	s_add_i32 s8, s5, s42
	s_ashr_i32 s1, s0, 31
	v_mov_b32_e32 v133, s9
	s_ashr_i32 s9, s8, 31
	s_lshl_b64 s[52:53], s[0:1], 3
	s_lshl_b64 s[54:55], s[0:1], 10
	s_lshl_b64 s[8:9], s[8:9], 13
	s_add_u32 s46, s46, s8
	s_addc_u32 s47, s47, s9
	s_lshl_b64 s[56:57], s[0:1], 13
	s_add_u32 s44, s44, s8
	v_cmp_eq_u32_e64 s[40:41], 0, v18
	s_addc_u32 s45, s45, s9
	s_branch .LBB0_618

.LBB0_625:
	s_setprio 0
	s_nop 0
	s_mul_i32 s0, s36, 6
	s_add_i32 s6, s0, 7
	s_cmp_ge_i32 s6, s69
	s_cbranch_scc1 .LBB0_675
	s_waitcnt vmcnt(0)
	s_waitcnt vmcnt(0)
	s_barrier
	s_mov_b64 s[0:1], exec
	v_readlane_b32 s4, v253, 16
	v_readlane_b32 s5, v253, 17
	s_and_b64 s[4:5], s[0:1], s[4:5]
	s_mov_b64 exec, s[4:5]
	s_cbranch_execz .LBB0_674
	v_readlane_b32 s4, v254, 2
	s_waitcnt vmcnt(0) expcnt(0) lgkmcnt(0)
	s_nop 0
	v_mov_b32_e32 v2, s4
	ds_read_b32 v5, v2
	ds_read_b32 v4, v2 offset:4
	s_waitcnt lgkmcnt(1)
	v_cmp_ne_u32_e32 vcc, 0, v5
	s_cbranch_vccnz .LBB0_642
	v_readlane_b32 s8, v254, 0
	v_readlane_b32 s9, v254, 1
	s_load_dwordx2 s[4:5], s[8:9], 0x4
	s_mov_b32 s37, 1
	s_waitcnt lgkmcnt(0)
	s_mul_i32 s27, s4, s33
	s_mul_i32 s27, s27, s5
	s_branch .LBB0_630
